# stack23 plus the separately validated work-reducing edits together: CV wait at first consumer, row-sum adds and P packing moved into P.V, E1 epilogue x4 folded into the reciprocal, K-loop counter SALU
# baseline (speedup 1.0000x reference)
; DI void finishSM(f32x16& p0, f32x16& p1, float alpha, float& l_reg, bf16x8& pa0, bf16x8& pa1, bf16x8& pa2, bf16x8& pa3) {
; #pragma unroll
;     for (int r = 0; r < 16; ++r) p1[r] = __builtin_amdgcn_exp2f(p1[r]);
;     float ps = 0;
; #pragma unroll
;     for (int r = 0; r < 16; ++r) ps += p0[r];
; #pragma unroll
;     for (int r = 0; r < 16; ++r) ps += p1[r];
;     { auto rr = __builtin_amdgcn_permlane32_swap(__float_as_uint(ps), __float_as_uint(ps), false, false); ps = __uint_as_float(rr[0]) + __uint_as_float(rr[1]); }
;     l_reg = l_reg * alpha + ps;
;     ...
;     AT_PK4(p0, 0, pa0); AT_PK4(p0, 8, pa1); AT_PK4(p1, 0, pa2); AT_PK4(p1, 8, pa3);
;     ...
; }
; DI void qkt(f32x16& p0, f32x16& p1, const char* Ks, const bf16x8* qr, const f32x16& negm, int r32, int hi) {
; #pragma unroll
;     for (int d0 = 0; d0 < 4; ++d0) { const int cb = (d0 * 16 + hi * 8) * 2;
;         const bf16x8 b0 = *reinterpret_cast<const bf16x8*>(Ks + AT_KSWZ(r32, cb));
;         const bf16x8 b1 = *reinterpret_cast<const bf16x8*>(Ks + AT_KSWZ(32 + r32, cb));
;         p0 = __builtin_amdgcn_mfma_f32_32x32x16_bf16(b0, qr[d0], d0 == 0 ? negm : p0, 0, 0, 0);
;         p1 = __builtin_amdgcn_mfma_f32_32x32x16_bf16(b1, qr[d0], d0 == 0 ? negm : p1, 0, 0, 0); }
; }
.LBB4_702:
	s_lshl_b32 s26, s66, 13
	s_add_i32 s26, s26, 0
	v_add_u32_e32 v72, s26, v205
	v_add_u32_e32 v112, s26, v206
	v_add_u32_e32 v180, s26, v207
	s_waitcnt lgkmcnt(1)
	v_mfma_f32_32x32x16_bf16 v[128:143], v[64:67], v[156:159], v[80:95]
	ds_read_b128 v[64:67], v72 offset:49152
	ds_read_b128 v[72:75], v72 offset:53248
	ds_read_b128 v[76:79], v112 offset:49152
	ds_read_b128 v[220:223], v112 offset:53248
	s_add_u32 s74, s46, s28
	s_addc_u32 s75, s47, s29
	s_add_u32 s78, s74, 0x23808000
	s_addc_u32 s79, s75, 0
	s_add_u32 s80, s74, 0x2380a000
	s_add_u32 s76, s46, s30
	s_addc_u32 s77, s47, s31
	s_add_u32 s82, s76, 0x21804000
	s_addc_u32 s83, s77, 0
	s_lshl_b32 s92, s64, 14
	s_add_i32 s92, s92, s94
	s_mov_b32 m0, s92
	s_lshl_b32 s96, s64, 13
	global_load_lds_dwordx4 v249, s[78:79]
	s_addk_i32 s92, 0x400
	s_mov_b32 m0, s92
	s_add_i32 s96, s96, s95
	global_load_lds_dwordx4 v250, s[78:79]
	s_nop 0
	s_mov_b32 m0, s96
	s_nop 0
	global_load_lds_dwordx4 v251, s[82:83]
	v_exp_f32_e32 v186, v97
	v_exp_f32_e32 v213, v98
	v_exp_f32_e32 v214, v99
	v_exp_f32_e32 v219, v100
	v_exp_f32_e32 v228, v101
	s_waitcnt lgkmcnt(4)
	v_mfma_f32_32x32x16_bf16 v[112:127], v[68:71], v[156:159], v[80:95]
	ds_read_b128 v[68:71], v180 offset:49152
	ds_read_b128 v[224:227], v180 offset:53248
	v_exp_f32_e32 v180, v96
	v_cvt_pk_bf16_f32 v96, v216, v218
	v_cvt_pk_bf16_f32 v97, v179, v217
	v_cvt_pk_bf16_f32 v98, v177, v215
	v_cvt_pk_bf16_f32 v99, v176, v178
	s_waitcnt lgkmcnt(4)
	v_mfma_f32_32x32x16_bf16 v[112:127], v[72:75], v[152:155], v[112:127]
	v_add_f32_e32 v75, 0, v216
	v_add_f32_e32 v75, v218, v75
	v_add_f32_e32 v75, v217, v75
	v_add_f32_e32 v75, v215, v75
	v_add_f32_e32 v75, v176, v75
	v_mfma_f32_32x32x16_bf16 v[128:143], v[64:67], v[152:155], v[128:143]
	v_add_f32_e32 v75, v172, v75
	s_waitcnt lgkmcnt(3)
	v_mfma_f32_32x32x16_bf16 v[128:143], v[76:79], v[148:151], v[128:143]
	v_add_f32_e32 v75, v180, v75
	v_add_f32_e32 v75, v186, v75
	v_exp_f32_e32 v64, v102
	v_exp_f32_e32 v65, v103
	v_exp_f32_e32 v66, v104
	s_waitcnt lgkmcnt(2)
	v_mfma_f32_32x32x16_bf16 v[112:127], v[220:223], v[148:151], v[112:127]
	v_exp_f32_e32 v67, v105
	v_exp_f32_e32 v105, v106
	v_exp_f32_e32 v106, v107
	v_exp_f32_e32 v107, v108
	v_exp_f32_e32 v72, v109
	v_exp_f32_e32 v73, v110
	v_exp_f32_e32 v74, v111
	s_waitcnt lgkmcnt(1)
	v_mfma_f32_32x32x16_bf16 v[128:143], v[68:71], v[144:147], v[128:143]
	v_add_f32_e32 v68, v213, v75
	v_add_f32_e32 v68, v214, v68
	v_add_f32_e32 v68, v219, v68
	v_add_f32_e32 v68, v228, v68
	v_add_f32_e32 v68, v64, v68
	v_add_f32_e32 v68, v65, v68
	v_add_f32_e32 v68, v66, v68
	v_add_f32_e32 v68, v67, v68
	s_waitcnt lgkmcnt(0)
	v_mfma_f32_32x32x16_bf16 v[112:127], v[224:227], v[144:147], v[112:127]
	v_add_f32_e32 v68, v105, v68
	v_add_f32_e32 v68, v106, v68
	v_add_f32_e32 v68, v107, v68
	v_add_f32_e32 v68, v72, v68
	v_add_f32_e32 v68, v73, v68
	v_add_f32_e32 v183, v74, v68
	v_cvt_pk_bf16_f32 v100, v180, v186
	v_cvt_pk_bf16_f32 v101, v213, v214
	v_cvt_pk_bf16_f32 v102, v219, v228
	v_cvt_pk_bf16_f32 v103, v64, v65
	v_cvt_pk_bf16_f32 v104, v66, v67
	v_cvt_pk_bf16_f32 v105, v105, v106
	v_cvt_pk_bf16_f32 v106, v107, v72
	v_cvt_pk_bf16_f32 v107, v73, v74
	s_addc_u32 s81, s75, 0
	s_andn2_b64 vcc, exec, s[2:3]
	s_cbranch_vccnz .LBB4_704
	s_mov_b64 s[2:3], s[8:9]
	global_store_dwordx2 v189, v[184:185], s[2:3] nt

; #define AT_SBAR() __builtin_amdgcn_sched_barrier(0)
; template <int OFF> DI s16x4 tr_read(int vb) { s16x4 r; asm volatile("ds_read_b64_tr_b16 %0, %1 offset:%2" : "=&v"(r) : "v"(vb), "i"(OFF) : "memory"); return r; }
; template <int D0> DI void pv_one(f32x16& od, int vb, bf16x8 pa0, bf16x8 pa1, bf16x8 pa2, bf16x8 pa3) {
;     const s16x4 l0 = tr_read<v_rd_off(D0, 0, 0)>(vb), h0 = tr_read<v_rd_off(D0, 0, 1)>(vb), l1 = tr_read<v_rd_off(D0, 1, 0)>(vb), h1 = tr_read<v_rd_off(D0, 1, 1)>(vb);
;     const s16x4 l2 = tr_read<v_rd_off(D0, 2, 0)>(vb), h2 = tr_read<v_rd_off(D0, 2, 1)>(vb), l3 = tr_read<v_rd_off(D0, 3, 0)>(vb), h3 = tr_read<v_rd_off(D0, 3, 1)>(vb);
;     asm volatile("s_waitcnt lgkmcnt(0)" ::: "memory"); AT_SBAR();
;     ...
;     od = __builtin_amdgcn_mfma_f32_32x32x16_bf16(AT_PK(l0, h0), pa0, od, 0, 0, 0);
;     od = __builtin_amdgcn_mfma_f32_32x32x16_bf16(AT_PK(l1, h1), pa1, od, 0, 0, 0);
;     od = __builtin_amdgcn_mfma_f32_32x32x16_bf16(AT_PK(l2, h2), pa2, od, 0, 0, 0);
;     od = __builtin_amdgcn_mfma_f32_32x32x16_bf16(AT_PK(l3, h3), pa3, od, 0, 0, 0);
.LBB4_706:
	ds_read_b64_tr_b16 v[214:215], v186 offset:0x600
	ds_read_b64_tr_b16 v[216:217], v186 offset:0x700
	ds_read_b64_tr_b16 v[218:219], v186 offset:0x1600
	ds_read_b64_tr_b16 v[220:221], v186 offset:0x1700
	ds_read_b64_tr_b16 v[222:223], v186 offset:0x2600
	ds_read_b64_tr_b16 v[224:225], v186 offset:0x2700
	ds_read_b64_tr_b16 v[226:227], v186 offset:0x3600
	ds_read_b64_tr_b16 v[228:229], v186 offset:0x3700
	s_waitcnt lgkmcnt(0)
	v_mfma_f32_32x32x16_bf16 v[0:15], v[214:217], v[96:99], v[0:15]
	s_lshl_b32 s2, s64, 14
	s_lshl_b32 s3, s64, 13
	s_sub_i32 s78, s2, s3
	v_mfma_f32_32x32x16_bf16 v[0:15], v[218:221], v[108:111], v[0:15]
	s_andn2_b64 s[2:3], exec, s[34:35]
	s_andn2_b64 vcc, exec, s[34:35]
	v_mfma_f32_32x32x16_bf16 v[0:15], v[222:225], v[100:103], v[0:15]
	v_mfma_f32_32x32x16_bf16 v[0:15], v[226:229], v[104:107], v[0:15]
	v_add_f32_e32 v254, v170, v254
	v_add_f32_e32 v183, v254, v183
	s_cbranch_vccnz .LBB4_711
	s_waitcnt vmcnt(3)
	v_med3_f32 v97, v160, -v255, v255
	v_med3_f32 v98, v164, -v255, v255
	v_cvt_scalef32_pk_fp8_f32 v99, v97, v98, s93
	v_med3_f32 v97, v161, -v255, v255
	v_med3_f32 v98, v165, -v255, v255
	v_cvt_scalef32_pk_fp8_f32 v100, v97, v98, s93
	v_med3_f32 v97, v162, -v255, v255
	v_med3_f32 v98, v166, -v255, v255
	s_bitcmp1_b32 s58, 0
	v_cvt_scalef32_pk_fp8_f32 v101, v97, v98, s93
	s_cselect_b32 s8, 0x1100, 0
	v_med3_f32 v97, v163, -v255, v255
	v_med3_f32 v98, v167, -v255, v255
	v_cmp_eq_u32_e32 vcc, 0, v181
	v_add_u32_e32 v96, s8, v191
	v_cvt_scalef32_pk_fp8_f32 v102, v97, v98, s93
	s_and_b64 vcc, exec, vcc
	s_and_b32 s34, s58, 31
	ds_write_b16 v96, v99
	ds_write_b16 v96, v100 offset:68
	ds_write_b16 v96, v101 offset:136
	ds_write_b16 v96, v102 offset:204
	s_cbranch_vccnz .LBB4_735
	s_lshl_b32 s8, s34, 7
	s_lshl_b32 s9, s58, 6
	s_and_b32 s8, s8, 0xf00
	s_and_b32 s9, s9, 64
	s_or_b32 s26, s8, s9
	s_cbranch_execnz .LBB4_710

; DI void finishSM(f32x16& p0, f32x16& p1, float alpha, float& l_reg, bf16x8& pa0, bf16x8& pa1, bf16x8& pa2, bf16x8& pa3) {
; #pragma unroll
;     for (int r = 0; r < 16; ++r) p1[r] = __builtin_amdgcn_exp2f(p1[r]);
;     float ps = 0;
; #pragma unroll
;     for (int r = 0; r < 16; ++r) ps += p0[r];
; #pragma unroll
;     for (int r = 0; r < 16; ++r) ps += p1[r];
;     { auto rr = __builtin_amdgcn_permlane32_swap(__float_as_uint(ps), __float_as_uint(ps), false, false); ps = __uint_as_float(rr[0]) + __uint_as_float(rr[1]); }
;     l_reg = l_reg * alpha + ps;
;     ...
;     AT_PK4(p0, 0, pa0); AT_PK4(p0, 8, pa1); AT_PK4(p1, 0, pa2); AT_PK4(p1, 8, pa3);
;     ...
; }
; DI void qkt(f32x16& p0, f32x16& p1, const char* Ks, const bf16x8* qr, const f32x16& negm, int r32, int hi) {
; #pragma unroll
;     for (int d0 = 0; d0 < 4; ++d0) { const int cb = (d0 * 16 + hi * 8) * 2;
;         const bf16x8 b0 = *reinterpret_cast<const bf16x8*>(Ks + AT_KSWZ(r32, cb));
;         const bf16x8 b1 = *reinterpret_cast<const bf16x8*>(Ks + AT_KSWZ(32 + r32, cb));
;         p0 = __builtin_amdgcn_mfma_f32_32x32x16_bf16(b0, qr[d0], d0 == 0 ? negm : p0, 0, 0, 0);
;         p1 = __builtin_amdgcn_mfma_f32_32x32x16_bf16(b1, qr[d0], d0 == 0 ? negm : p1, 0, 0, 0); }
; }
.LBB4_723:
	v_exp_f32_e32 v186, v128
	v_exp_f32_e32 v230, v129
	v_exp_f32_e32 v231, v130
	v_exp_f32_e32 v232, v131
	v_exp_f32_e32 v233, v132
	v_exp_f32_e32 v234, v133
	v_exp_f32_e32 v235, v134
	v_exp_f32_e32 v236, v135
	v_exp_f32_e32 v237, v136
	v_exp_f32_e32 v238, v137
	v_exp_f32_e32 v239, v138
	v_exp_f32_e32 v240, v139
	v_exp_f32_e32 v241, v140
	v_exp_f32_e32 v242, v141
	v_exp_f32_e32 v243, v142
	v_exp_f32_e32 v244, v143
	v_add_u32_e32 v101, s78, v205
	v_add_u32_e32 v102, s78, v206
	v_add_u32_e32 v103, s78, v207
	ds_read_b128 v[172:175], v101 offset:49152
	ds_read_b128 v[176:179], v101 offset:53248
	ds_read_b128 v[214:217], v102 offset:49152
	ds_read_b128 v[218:221], v102 offset:53248
	ds_read_b128 v[222:225], v103 offset:49152
	ds_read_b128 v[226:229], v103 offset:53248
	v_exp_f32_e32 v112, v112
	v_exp_f32_e32 v113, v113
	v_exp_f32_e32 v114, v114
	s_waitcnt lgkmcnt(7)
	v_mfma_f32_32x32x16_bf16 v[128:143], v[96:99], v[156:159], v[80:95]
	s_add_u32 s78, s74, 0x2380c000
	s_addc_u32 s79, s75, 0
	s_add_u32 s74, s74, 0x2380e000
	s_addc_u32 s75, s75, 0
	s_add_u32 s76, s76, 0x21806000
	s_addc_u32 s77, s77, 0
	s_lshl_b32 s92, s65, 14
	s_add_i32 s92, s92, s94
	s_mov_b32 m0, s92
	s_lshl_b32 s96, s65, 13
	global_load_lds_dwordx4 v249, s[78:79]
	s_addk_i32 s92, 0x400
	s_mov_b32 m0, s92
	s_add_i32 s96, s96, s95
	global_load_lds_dwordx4 v250, s[78:79]
	s_nop 0
	s_mov_b32 m0, s96
	s_nop 0
	global_load_lds_dwordx4 v251, s[76:77]
	s_nop 0
	v_exp_f32_e32 v115, v115
	v_exp_f32_e32 v116, v116
	v_exp_f32_e32 v117, v117
	v_exp_f32_e32 v118, v118
	v_exp_f32_e32 v119, v119
	s_waitcnt lgkmcnt(6)
	v_mfma_f32_32x32x16_bf16 v[96:111], v[168:171], v[156:159], v[80:95]
	v_exp_f32_e32 v168, v120
	v_add_f32_e32 v120, 0, v186
	v_add_f32_e32 v120, v230, v120
	v_add_f32_e32 v120, v231, v120
	v_add_f32_e32 v120, v232, v120
	v_add_f32_e32 v120, v233, v120
	v_add_f32_e32 v120, v234, v120
	v_add_f32_e32 v120, v235, v120
	v_add_f32_e32 v120, v236, v120
	v_add_f32_e32 v120, v237, v120
	v_add_f32_e32 v120, v238, v120
	s_waitcnt lgkmcnt(5)
	v_mfma_f32_32x32x16_bf16 v[128:143], v[172:175], v[152:155], v[128:143]
	v_add_f32_e32 v120, v239, v120
	v_add_f32_e32 v120, v240, v120
	v_add_f32_e32 v120, v241, v120
	v_add_f32_e32 v120, v242, v120
	v_add_f32_e32 v120, v243, v120
	v_add_f32_e32 v120, v244, v120
	v_add_f32_e32 v120, v112, v120
	s_waitcnt lgkmcnt(4)
	v_mfma_f32_32x32x16_bf16 v[96:111], v[176:179], v[152:155], v[96:111]
	v_add_f32_e32 v120, v113, v120
	v_add_f32_e32 v120, v114, v120
	v_add_f32_e32 v120, v115, v120
	v_add_f32_e32 v120, v116, v120
	v_exp_f32_e32 v169, v121
	v_add_f32_e32 v120, v117, v120
	v_exp_f32_e32 v170, v122
	s_waitcnt lgkmcnt(3)
	v_mfma_f32_32x32x16_bf16 v[128:143], v[214:217], v[148:151], v[128:143]
	v_add_f32_e32 v120, v118, v120
	v_exp_f32_e32 v171, v123
	v_add_f32_e32 v120, v119, v120
	v_exp_f32_e32 v172, v124
	v_exp_f32_e32 v173, v125
	s_waitcnt lgkmcnt(2)
	v_mfma_f32_32x32x16_bf16 v[96:111], v[218:221], v[148:151], v[96:111]
	v_exp_f32_e32 v174, v126
	v_exp_f32_e32 v175, v127
	v_add_f32_e32 v120, v174, v120
	s_waitcnt lgkmcnt(1)
	v_mfma_f32_32x32x16_bf16 v[128:143], v[222:225], v[144:147], v[128:143]
	v_add_f32_e32 v213, v175, v120
	v_cvt_pk_bf16_f32 v120, v186, v230
	v_cvt_pk_bf16_f32 v121, v231, v232
	v_cvt_pk_bf16_f32 v122, v233, v234
	v_cvt_pk_bf16_f32 v123, v235, v236
	v_cvt_pk_bf16_f32 v124, v237, v238
	s_waitcnt lgkmcnt(0)
	v_mfma_f32_32x32x16_bf16 v[96:111], v[226:229], v[144:147], v[96:111]
	v_cvt_pk_bf16_f32 v125, v239, v240
	v_cvt_pk_bf16_f32 v126, v241, v242
	v_cvt_pk_bf16_f32 v127, v243, v244
	v_cvt_pk_bf16_f32 v112, v112, v113
	v_cvt_pk_bf16_f32 v113, v114, v115
	v_cvt_pk_bf16_f32 v114, v116, v117
	v_cvt_pk_bf16_f32 v115, v118, v119
	s_and_b64 vcc, exec, s[2:3]
	s_cbranch_vccnz .LBB4_725
	s_mov_b64 s[2:3], s[8:9]
	global_store_dwordx2 v189, v[184:185], s[2:3] nt

; #define AT_SBAR() __builtin_amdgcn_sched_barrier(0)
; template <int OFF> DI s16x4 tr_read(int vb) { s16x4 r; asm volatile("ds_read_b64_tr_b16 %0, %1 offset:%2" : "=&v"(r) : "v"(vb), "i"(OFF) : "memory"); return r; }
; template <int D0> DI void pv_one(f32x16& od, int vb, bf16x8 pa0, bf16x8 pa1, bf16x8 pa2, bf16x8 pa3) {
;     const s16x4 l0 = tr_read<v_rd_off(D0, 0, 0)>(vb), h0 = tr_read<v_rd_off(D0, 0, 1)>(vb), l1 = tr_read<v_rd_off(D0, 1, 0)>(vb), h1 = tr_read<v_rd_off(D0, 1, 1)>(vb);
;     const s16x4 l2 = tr_read<v_rd_off(D0, 2, 0)>(vb), h2 = tr_read<v_rd_off(D0, 2, 1)>(vb), l3 = tr_read<v_rd_off(D0, 3, 0)>(vb), h3 = tr_read<v_rd_off(D0, 3, 1)>(vb);
;     asm volatile("s_waitcnt lgkmcnt(0)" ::: "memory"); AT_SBAR();
;     ...
;     od = __builtin_amdgcn_mfma_f32_32x32x16_bf16(AT_PK(l0, h0), pa0, od, 0, 0, 0);
;     od = __builtin_amdgcn_mfma_f32_32x32x16_bf16(AT_PK(l1, h1), pa1, od, 0, 0, 0);
;     od = __builtin_amdgcn_mfma_f32_32x32x16_bf16(AT_PK(l2, h2), pa2, od, 0, 0, 0);
;     od = __builtin_amdgcn_mfma_f32_32x32x16_bf16(AT_PK(l3, h3), pa3, od, 0, 0, 0);
.LBB4_726:
	ds_read_b64_tr_b16 v[216:217], v215 offset:0x600
	ds_read_b64_tr_b16 v[218:219], v215 offset:0x700
	ds_read_b64_tr_b16 v[220:221], v215 offset:0x1600
	ds_read_b64_tr_b16 v[222:223], v215 offset:0x1700
	ds_read_b64_tr_b16 v[224:225], v215 offset:0x2600
	ds_read_b64_tr_b16 v[226:227], v215 offset:0x2700
	ds_read_b64_tr_b16 v[228:229], v215 offset:0x3600
	ds_read_b64_tr_b16 v[230:231], v215 offset:0x3700
	s_waitcnt lgkmcnt(0)
	v_mfma_f32_32x32x16_bf16 v[0:15], v[216:219], v[120:123], v[0:15]
	s_add_i32 s2, s67, 0
	s_mov_b32 s26, 0
	s_andn2_b64 vcc, exec, s[34:35]
	v_mfma_f32_32x32x16_bf16 v[0:15], v[220:223], v[124:127], v[0:15]
	v_mfma_f32_32x32x16_bf16 v[0:15], v[224:227], v[112:115], v[0:15]
	s_andn2_b64 s[2:3], exec, s[34:35]
	v_mfma_f32_32x32x16_bf16 v[0:15], v[228:231], v[116:119], v[0:15]
	v_add_f32_e32 v254, v173, v254
	v_add_f32_e32 v213, v254, v213
	s_cbranch_vccnz .LBB4_731
	s_waitcnt vmcnt(3)
	v_med3_f32 v113, v160, -v255, v255
	v_med3_f32 v114, v164, -v255, v255
	v_cvt_scalef32_pk_fp8_f32 v115, v113, v114, s93
	v_med3_f32 v113, v161, -v255, v255
	v_med3_f32 v114, v165, -v255, v255
	v_cvt_scalef32_pk_fp8_f32 v116, v113, v114, s93
	v_med3_f32 v113, v162, -v255, v255
	v_med3_f32 v114, v166, -v255, v255
	s_bitcmp1_b32 s58, 0
	v_cvt_scalef32_pk_fp8_f32 v117, v113, v114, s93
	s_cselect_b32 s8, 0x1100, 0
	v_med3_f32 v113, v163, -v255, v255
	v_med3_f32 v114, v167, -v255, v255
	v_cmp_eq_u32_e32 vcc, 0, v181
	v_add_u32_e32 v112, s8, v191
	v_cvt_scalef32_pk_fp8_f32 v118, v113, v114, s93
	s_and_b64 vcc, exec, vcc
	s_and_b32 s37, s58, 31
	ds_write_b16 v112, v115
	ds_write_b16 v112, v116 offset:68
	ds_write_b16 v112, v117 offset:136
	ds_write_b16 v112, v118 offset:204
	s_cbranch_vccnz .LBB4_736
	s_lshl_b32 s8, s37, 7
	s_lshl_b32 s9, s58, 6
	s_and_b32 s8, s8, 0xf00
	s_and_b32 s9, s9, 64
	s_or_b32 s26, s8, s9
	s_cbranch_execnz .LBB4_730

; DI void finishSM(f32x16& p0, f32x16& p1, float alpha, float& l_reg, bf16x8& pa0, bf16x8& pa1, bf16x8& pa2, bf16x8& pa3) {
; #pragma unroll
;     for (int r = 0; r < 16; ++r) p1[r] = __builtin_amdgcn_exp2f(p1[r]);
;     float ps = 0;
; #pragma unroll
;     for (int r = 0; r < 16; ++r) ps += p0[r];
; #pragma unroll
;     for (int r = 0; r < 16; ++r) ps += p1[r];
;     { auto rr = __builtin_amdgcn_permlane32_swap(__float_as_uint(ps), __float_as_uint(ps), false, false); ps = __uint_as_float(rr[0]) + __uint_as_float(rr[1]); }
;     l_reg = l_reg * alpha + ps;
;     ...
;     AT_PK4(p0, 0, pa0); AT_PK4(p0, 8, pa1); AT_PK4(p1, 0, pa2); AT_PK4(p1, 8, pa3);
;     ...
; }
; DI void qkt(f32x16& p0, f32x16& p1, const char* Ks, const bf16x8* qr, const f32x16& negm, int r32, int hi) {
; #pragma unroll
;     for (int d0 = 0; d0 < 4; ++d0) { const int cb = (d0 * 16 + hi * 8) * 2;
;         const bf16x8 b0 = *reinterpret_cast<const bf16x8*>(Ks + AT_KSWZ(r32, cb));
;         const bf16x8 b1 = *reinterpret_cast<const bf16x8*>(Ks + AT_KSWZ(32 + r32, cb));
;         p0 = __builtin_amdgcn_mfma_f32_32x32x16_bf16(b0, qr[d0], d0 == 0 ? negm : p0, 0, 0, 0);
;         p1 = __builtin_amdgcn_mfma_f32_32x32x16_bf16(b1, qr[d0], d0 == 0 ? negm : p1, 0, 0, 0); }
; }
.LBB4_775:
	s_lshl_b32 s20, s30, 13
	s_add_i32 s20, s20, 0
	v_add_u32_e32 v72, s20, v208
	v_add_u32_e32 v112, s20, v209
	v_add_u32_e32 v180, s20, v210
	s_waitcnt lgkmcnt(1)
	v_mfma_f32_32x32x16_bf16 v[128:143], v[64:67], v[156:159], v[80:95]
	ds_read_b128 v[64:67], v72 offset:49152
	ds_read_b128 v[72:75], v72 offset:53248
	ds_read_b128 v[76:79], v112 offset:49152
	ds_read_b128 v[224:227], v112 offset:53248
	s_add_u32 s34, s46, s16
	s_addc_u32 s35, s47, s17
	s_add_u32 s24, s34, 0x23808000
	s_addc_u32 s25, s35, 0
	s_add_u32 s66, s34, 0x2380a000
	s_add_u32 s37, s46, s18
	s_addc_u32 s64, s47, s19
	s_add_u32 s74, s37, 0x21884000
	s_addc_u32 s75, s64, 0
	s_lshl_b32 s92, s15, 14
	s_add_i32 s92, s92, s94
	s_mov_b32 m0, s92
	s_lshl_b32 s96, s15, 13
	global_load_lds_dwordx4 v249, s[24:25]
	s_addk_i32 s92, 0x400
	s_mov_b32 m0, s92
	s_add_i32 s96, s96, s95
	global_load_lds_dwordx4 v250, s[24:25]
	s_nop 0
	s_mov_b32 m0, s96
	s_nop 0
	global_load_lds_dwordx4 v251, s[74:75]
	v_exp_f32_e32 v182, v97
	v_exp_f32_e32 v217, v98
	v_exp_f32_e32 v218, v99
	v_exp_f32_e32 v223, v100
	v_exp_f32_e32 v232, v101
	s_waitcnt lgkmcnt(4)
	v_mfma_f32_32x32x16_bf16 v[112:127], v[68:71], v[156:159], v[80:95]
	ds_read_b128 v[68:71], v180 offset:49152
	ds_read_b128 v[228:231], v180 offset:53248
	v_exp_f32_e32 v180, v96
	v_cvt_pk_bf16_f32 v96, v220, v222
	v_cvt_pk_bf16_f32 v97, v179, v221
	v_cvt_pk_bf16_f32 v98, v177, v219
	v_cvt_pk_bf16_f32 v99, v176, v178
	s_waitcnt lgkmcnt(4)
	v_mfma_f32_32x32x16_bf16 v[112:127], v[72:75], v[152:155], v[112:127]
	v_add_f32_e32 v75, 0, v220
	v_add_f32_e32 v75, v222, v75
	v_add_f32_e32 v75, v221, v75
	v_add_f32_e32 v75, v219, v75
	v_add_f32_e32 v75, v176, v75
	v_mfma_f32_32x32x16_bf16 v[128:143], v[64:67], v[152:155], v[128:143]
	v_add_f32_e32 v75, v172, v75
	s_waitcnt lgkmcnt(3)
	v_mfma_f32_32x32x16_bf16 v[128:143], v[76:79], v[148:151], v[128:143]
	v_add_f32_e32 v75, v180, v75
	v_add_f32_e32 v75, v182, v75
	v_exp_f32_e32 v64, v102
	v_exp_f32_e32 v65, v103
	v_exp_f32_e32 v66, v104
	s_waitcnt lgkmcnt(2)
	v_mfma_f32_32x32x16_bf16 v[112:127], v[224:227], v[148:151], v[112:127]
	v_exp_f32_e32 v67, v105
	v_exp_f32_e32 v105, v106
	v_exp_f32_e32 v106, v107
	v_exp_f32_e32 v107, v108
	v_exp_f32_e32 v72, v109
	v_exp_f32_e32 v73, v110
	v_exp_f32_e32 v74, v111
	s_waitcnt lgkmcnt(1)
	v_mfma_f32_32x32x16_bf16 v[128:143], v[68:71], v[144:147], v[128:143]
	v_add_f32_e32 v68, v217, v75
	v_add_f32_e32 v68, v218, v68
	v_add_f32_e32 v68, v223, v68
	v_add_f32_e32 v68, v232, v68
	v_add_f32_e32 v68, v64, v68
	v_add_f32_e32 v68, v65, v68
	v_add_f32_e32 v68, v66, v68
	v_add_f32_e32 v68, v67, v68
	s_waitcnt lgkmcnt(0)
	v_mfma_f32_32x32x16_bf16 v[112:127], v[228:231], v[144:147], v[112:127]
	v_add_f32_e32 v68, v105, v68
	v_add_f32_e32 v68, v106, v68
	v_add_f32_e32 v68, v107, v68
	v_add_f32_e32 v68, v72, v68
	v_add_f32_e32 v68, v73, v68
	v_add_f32_e32 v215, v74, v68
	v_cvt_pk_bf16_f32 v100, v180, v182
	v_cvt_pk_bf16_f32 v101, v217, v218
	v_cvt_pk_bf16_f32 v102, v223, v232
	v_cvt_pk_bf16_f32 v103, v64, v65
	v_cvt_pk_bf16_f32 v104, v66, v67
	v_cvt_pk_bf16_f32 v105, v105, v106
	v_cvt_pk_bf16_f32 v106, v107, v72
	v_cvt_pk_bf16_f32 v107, v73, v74
	s_addc_u32 s67, s35, 0
	s_andn2_b64 vcc, exec, s[2:3]
	s_cbranch_vccnz .LBB4_777
	s_mov_b64 s[2:3], s[8:9]
	global_store_dwordx2 v193, v[184:185], s[2:3] nt

; #define AT_SBAR() __builtin_amdgcn_sched_barrier(0)
; template <int OFF> DI s16x4 tr_read(int vb) { s16x4 r; asm volatile("ds_read_b64_tr_b16 %0, %1 offset:%2" : "=&v"(r) : "v"(vb), "i"(OFF) : "memory"); return r; }
; template <int D0> DI void pv_one(f32x16& od, int vb, bf16x8 pa0, bf16x8 pa1, bf16x8 pa2, bf16x8 pa3) {
;     const s16x4 l0 = tr_read<v_rd_off(D0, 0, 0)>(vb), h0 = tr_read<v_rd_off(D0, 0, 1)>(vb), l1 = tr_read<v_rd_off(D0, 1, 0)>(vb), h1 = tr_read<v_rd_off(D0, 1, 1)>(vb);
;     const s16x4 l2 = tr_read<v_rd_off(D0, 2, 0)>(vb), h2 = tr_read<v_rd_off(D0, 2, 1)>(vb), l3 = tr_read<v_rd_off(D0, 3, 0)>(vb), h3 = tr_read<v_rd_off(D0, 3, 1)>(vb);
;     asm volatile("s_waitcnt lgkmcnt(0)" ::: "memory"); AT_SBAR();
;     ...
;     od = __builtin_amdgcn_mfma_f32_32x32x16_bf16(AT_PK(l0, h0), pa0, od, 0, 0, 0);
;     od = __builtin_amdgcn_mfma_f32_32x32x16_bf16(AT_PK(l1, h1), pa1, od, 0, 0, 0);
;     od = __builtin_amdgcn_mfma_f32_32x32x16_bf16(AT_PK(l2, h2), pa2, od, 0, 0, 0);
;     od = __builtin_amdgcn_mfma_f32_32x32x16_bf16(AT_PK(l3, h3), pa3, od, 0, 0, 0);
.LBB4_779:
	ds_read_b64_tr_b16 v[218:219], v182 offset:0x600
	ds_read_b64_tr_b16 v[220:221], v182 offset:0x700
	ds_read_b64_tr_b16 v[222:223], v182 offset:0x1600
	ds_read_b64_tr_b16 v[224:225], v182 offset:0x1700
	ds_read_b64_tr_b16 v[226:227], v182 offset:0x2600
	ds_read_b64_tr_b16 v[228:229], v182 offset:0x2700
	ds_read_b64_tr_b16 v[230:231], v182 offset:0x3600
	ds_read_b64_tr_b16 v[232:233], v182 offset:0x3700
	s_waitcnt lgkmcnt(0)
	v_mfma_f32_32x32x16_bf16 v[0:15], v[218:221], v[96:99], v[0:15]
	s_lshl_b32 s2, s15, 14
	s_lshl_b32 s3, s15, 13
	s_sub_i32 s65, s2, s3
	v_mfma_f32_32x32x16_bf16 v[0:15], v[222:225], v[108:111], v[0:15]
	s_andn2_b64 s[2:3], exec, s[22:23]
	s_andn2_b64 vcc, exec, s[22:23]
	v_mfma_f32_32x32x16_bf16 v[0:15], v[226:229], v[100:103], v[0:15]
	v_mfma_f32_32x32x16_bf16 v[0:15], v[230:233], v[104:107], v[0:15]
	v_add_f32_e32 v254, v170, v254
	v_add_f32_e32 v215, v254, v215
	s_cbranch_vccnz .LBB4_784
	s_waitcnt vmcnt(3)
	v_med3_f32 v97, v160, -v255, v255
	v_med3_f32 v98, v164, -v255, v255
	v_cvt_scalef32_pk_fp8_f32 v99, v97, v98, s93
	v_med3_f32 v97, v161, -v255, v255
	v_med3_f32 v98, v165, -v255, v255
	v_cvt_scalef32_pk_fp8_f32 v100, v97, v98, s93
	v_med3_f32 v97, v162, -v255, v255
	v_med3_f32 v98, v166, -v255, v255
	s_bitcmp1_b32 s58, 0
	v_cvt_scalef32_pk_fp8_f32 v101, v97, v98, s93
	s_cselect_b32 s8, 0x1100, 0
	v_med3_f32 v97, v163, -v255, v255
	v_med3_f32 v98, v167, -v255, v255
	v_cmp_eq_u32_e32 vcc, 0, v181
	v_add_u32_e32 v96, s8, v195
	v_cvt_scalef32_pk_fp8_f32 v102, v97, v98, s93
	s_and_b64 vcc, exec, vcc
	s_and_b32 s22, s58, 31
	ds_write_b16 v96, v99
	ds_write_b16 v96, v100 offset:68
	ds_write_b16 v96, v101 offset:136
	ds_write_b16 v96, v102 offset:204
	s_cbranch_vccnz .LBB4_808
	s_lshl_b32 s8, s22, 7
	s_lshl_b32 s9, s58, 6
	s_and_b32 s8, s8, 0xf00
	s_and_b32 s9, s9, 64
	s_or_b32 s20, s8, s9
	s_cbranch_execnz .LBB4_783

; DI void finishSM(f32x16& p0, f32x16& p1, float alpha, float& l_reg, bf16x8& pa0, bf16x8& pa1, bf16x8& pa2, bf16x8& pa3) {
; #pragma unroll
;     for (int r = 0; r < 16; ++r) p1[r] = __builtin_amdgcn_exp2f(p1[r]);
;     float ps = 0;
; #pragma unroll
;     for (int r = 0; r < 16; ++r) ps += p0[r];
; #pragma unroll
;     for (int r = 0; r < 16; ++r) ps += p1[r];
;     { auto rr = __builtin_amdgcn_permlane32_swap(__float_as_uint(ps), __float_as_uint(ps), false, false); ps = __uint_as_float(rr[0]) + __uint_as_float(rr[1]); }
;     l_reg = l_reg * alpha + ps;
;     ...
;     AT_PK4(p0, 0, pa0); AT_PK4(p0, 8, pa1); AT_PK4(p1, 0, pa2); AT_PK4(p1, 8, pa3);
;     ...
; }
; DI void qkt(f32x16& p0, f32x16& p1, const char* Ks, const bf16x8* qr, const f32x16& negm, int r32, int hi) {
; #pragma unroll
;     for (int d0 = 0; d0 < 4; ++d0) { const int cb = (d0 * 16 + hi * 8) * 2;
;         const bf16x8 b0 = *reinterpret_cast<const bf16x8*>(Ks + AT_KSWZ(r32, cb));
;         const bf16x8 b1 = *reinterpret_cast<const bf16x8*>(Ks + AT_KSWZ(32 + r32, cb));
;         p0 = __builtin_amdgcn_mfma_f32_32x32x16_bf16(b0, qr[d0], d0 == 0 ? negm : p0, 0, 0, 0);
;         p1 = __builtin_amdgcn_mfma_f32_32x32x16_bf16(b1, qr[d0], d0 == 0 ? negm : p1, 0, 0, 0); }
; }
.LBB4_796:
	v_exp_f32_e32 v182, v128
	v_exp_f32_e32 v234, v129
	v_exp_f32_e32 v235, v130
	v_exp_f32_e32 v236, v131
	v_exp_f32_e32 v237, v132
	v_exp_f32_e32 v238, v133
	v_exp_f32_e32 v239, v134
	v_exp_f32_e32 v240, v135
	v_exp_f32_e32 v241, v136
	v_exp_f32_e32 v242, v137
	v_exp_f32_e32 v243, v138
	v_exp_f32_e32 v244, v139
	v_exp_f32_e32 v245, v140
	v_exp_f32_e32 v246, v141
	v_exp_f32_e32 v247, v142
	v_exp_f32_e32 v248, v143
	v_add_u32_e32 v101, s65, v208
	v_add_u32_e32 v102, s65, v209
	v_add_u32_e32 v103, s65, v210
	ds_read_b128 v[172:175], v101 offset:49152
	ds_read_b128 v[176:179], v101 offset:53248
	ds_read_b128 v[218:221], v102 offset:49152
	ds_read_b128 v[222:225], v102 offset:53248
	ds_read_b128 v[226:229], v103 offset:49152
	ds_read_b128 v[230:233], v103 offset:53248
	v_exp_f32_e32 v112, v112
	v_exp_f32_e32 v113, v113
	v_exp_f32_e32 v114, v114
	s_waitcnt lgkmcnt(7)
	v_mfma_f32_32x32x16_bf16 v[128:143], v[96:99], v[156:159], v[80:95]
	s_add_u32 s24, s34, 0x2380c000
	s_addc_u32 s25, s35, 0
	s_add_u32 s34, s34, 0x2380e000
	s_addc_u32 s35, s35, 0
	s_add_u32 s66, s37, 0x21886000
	s_addc_u32 s67, s64, 0
	s_lshl_b32 s92, s29, 14
	s_add_i32 s92, s92, s94
	s_mov_b32 m0, s92
	s_lshl_b32 s96, s29, 13
	global_load_lds_dwordx4 v249, s[24:25]
	s_addk_i32 s92, 0x400
	s_mov_b32 m0, s92
	s_add_i32 s96, s96, s95
	global_load_lds_dwordx4 v250, s[24:25]
	s_nop 0
	s_mov_b32 m0, s96
	s_nop 0
	global_load_lds_dwordx4 v251, s[66:67]
	s_nop 0
	v_exp_f32_e32 v115, v115
	v_exp_f32_e32 v116, v116
	v_exp_f32_e32 v117, v117
	v_exp_f32_e32 v118, v118
	v_exp_f32_e32 v119, v119
	s_waitcnt lgkmcnt(6)
	v_mfma_f32_32x32x16_bf16 v[96:111], v[168:171], v[156:159], v[80:95]
	v_exp_f32_e32 v168, v120
	v_add_f32_e32 v120, 0, v182
	v_add_f32_e32 v120, v234, v120
	v_add_f32_e32 v120, v235, v120
	v_add_f32_e32 v120, v236, v120
	v_add_f32_e32 v120, v237, v120
	v_add_f32_e32 v120, v238, v120
	v_add_f32_e32 v120, v239, v120
	v_add_f32_e32 v120, v240, v120
	v_add_f32_e32 v120, v241, v120
	v_add_f32_e32 v120, v242, v120
	s_waitcnt lgkmcnt(5)
	v_mfma_f32_32x32x16_bf16 v[128:143], v[172:175], v[152:155], v[128:143]
	v_add_f32_e32 v120, v243, v120
	v_add_f32_e32 v120, v244, v120
	v_add_f32_e32 v120, v245, v120
	v_add_f32_e32 v120, v246, v120
	v_add_f32_e32 v120, v247, v120
	v_add_f32_e32 v120, v248, v120
	v_add_f32_e32 v120, v112, v120
	s_waitcnt lgkmcnt(4)
	v_mfma_f32_32x32x16_bf16 v[96:111], v[176:179], v[152:155], v[96:111]
	v_add_f32_e32 v120, v113, v120
	v_add_f32_e32 v120, v114, v120
	v_add_f32_e32 v120, v115, v120
	v_add_f32_e32 v120, v116, v120
	v_exp_f32_e32 v169, v121
	v_add_f32_e32 v120, v117, v120
	v_exp_f32_e32 v170, v122
	s_waitcnt lgkmcnt(3)
	v_mfma_f32_32x32x16_bf16 v[128:143], v[218:221], v[148:151], v[128:143]
	v_add_f32_e32 v120, v118, v120
	v_exp_f32_e32 v171, v123
	v_add_f32_e32 v120, v119, v120
	v_exp_f32_e32 v172, v124
	v_exp_f32_e32 v173, v125
	s_waitcnt lgkmcnt(2)
	v_mfma_f32_32x32x16_bf16 v[96:111], v[222:225], v[148:151], v[96:111]
	v_exp_f32_e32 v174, v126
	v_exp_f32_e32 v175, v127
	v_add_f32_e32 v120, v174, v120
	s_waitcnt lgkmcnt(1)
	v_mfma_f32_32x32x16_bf16 v[128:143], v[226:229], v[144:147], v[128:143]
	v_add_f32_e32 v217, v175, v120
	v_cvt_pk_bf16_f32 v120, v182, v234
	v_cvt_pk_bf16_f32 v121, v235, v236
	v_cvt_pk_bf16_f32 v122, v237, v238
	v_cvt_pk_bf16_f32 v123, v239, v240
	v_cvt_pk_bf16_f32 v124, v241, v242
	s_waitcnt lgkmcnt(0)
	v_mfma_f32_32x32x16_bf16 v[96:111], v[230:233], v[144:147], v[96:111]
	v_cvt_pk_bf16_f32 v125, v243, v244
	v_cvt_pk_bf16_f32 v126, v245, v246
	v_cvt_pk_bf16_f32 v127, v247, v248
	v_cvt_pk_bf16_f32 v112, v112, v113
	v_cvt_pk_bf16_f32 v113, v114, v115
	v_cvt_pk_bf16_f32 v114, v116, v117
	v_cvt_pk_bf16_f32 v115, v118, v119
	s_and_b64 vcc, exec, s[2:3]
	s_cbranch_vccnz .LBB4_798
	s_mov_b64 s[2:3], s[8:9]
	global_store_dwordx2 v193, v[184:185], s[2:3] nt

; #define AT_SBAR() __builtin_amdgcn_sched_barrier(0)
; template <int OFF> DI s16x4 tr_read(int vb) { s16x4 r; asm volatile("ds_read_b64_tr_b16 %0, %1 offset:%2" : "=&v"(r) : "v"(vb), "i"(OFF) : "memory"); return r; }
; template <int D0> DI void pv_one(f32x16& od, int vb, bf16x8 pa0, bf16x8 pa1, bf16x8 pa2, bf16x8 pa3) {
;     const s16x4 l0 = tr_read<v_rd_off(D0, 0, 0)>(vb), h0 = tr_read<v_rd_off(D0, 0, 1)>(vb), l1 = tr_read<v_rd_off(D0, 1, 0)>(vb), h1 = tr_read<v_rd_off(D0, 1, 1)>(vb);
;     const s16x4 l2 = tr_read<v_rd_off(D0, 2, 0)>(vb), h2 = tr_read<v_rd_off(D0, 2, 1)>(vb), l3 = tr_read<v_rd_off(D0, 3, 0)>(vb), h3 = tr_read<v_rd_off(D0, 3, 1)>(vb);
;     asm volatile("s_waitcnt lgkmcnt(0)" ::: "memory"); AT_SBAR();
;     ...
;     od = __builtin_amdgcn_mfma_f32_32x32x16_bf16(AT_PK(l0, h0), pa0, od, 0, 0, 0);
;     od = __builtin_amdgcn_mfma_f32_32x32x16_bf16(AT_PK(l1, h1), pa1, od, 0, 0, 0);
;     od = __builtin_amdgcn_mfma_f32_32x32x16_bf16(AT_PK(l2, h2), pa2, od, 0, 0, 0);
;     od = __builtin_amdgcn_mfma_f32_32x32x16_bf16(AT_PK(l3, h3), pa3, od, 0, 0, 0);
.LBB4_799:
	ds_read_b64_tr_b16 v[220:221], v219 offset:0x600
	ds_read_b64_tr_b16 v[222:223], v219 offset:0x700
	ds_read_b64_tr_b16 v[224:225], v219 offset:0x1600
	ds_read_b64_tr_b16 v[226:227], v219 offset:0x1700
	ds_read_b64_tr_b16 v[228:229], v219 offset:0x2600
	ds_read_b64_tr_b16 v[230:231], v219 offset:0x2700
	ds_read_b64_tr_b16 v[232:233], v219 offset:0x3600
	ds_read_b64_tr_b16 v[234:235], v219 offset:0x3700
	s_waitcnt lgkmcnt(0)
	v_mfma_f32_32x32x16_bf16 v[0:15], v[220:223], v[120:123], v[0:15]
	s_add_i32 s2, s31, 0
	s_mov_b32 s20, 0
	s_andn2_b64 vcc, exec, s[22:23]
	v_mfma_f32_32x32x16_bf16 v[0:15], v[224:227], v[124:127], v[0:15]
	v_mfma_f32_32x32x16_bf16 v[0:15], v[228:231], v[112:115], v[0:15]
	s_andn2_b64 s[2:3], exec, s[22:23]
	v_mfma_f32_32x32x16_bf16 v[0:15], v[232:235], v[116:119], v[0:15]
	v_add_f32_e32 v254, v173, v254
	v_add_f32_e32 v217, v254, v217
	s_cbranch_vccnz .LBB4_804
	s_waitcnt vmcnt(3)
	v_med3_f32 v113, v160, -v255, v255
	v_med3_f32 v114, v164, -v255, v255
	v_cvt_scalef32_pk_fp8_f32 v115, v113, v114, s93
	v_med3_f32 v113, v161, -v255, v255
	v_med3_f32 v114, v165, -v255, v255
	v_cvt_scalef32_pk_fp8_f32 v116, v113, v114, s93
	v_med3_f32 v113, v162, -v255, v255
	v_med3_f32 v114, v166, -v255, v255
	s_bitcmp1_b32 s58, 0
	v_cvt_scalef32_pk_fp8_f32 v117, v113, v114, s93
	s_cselect_b32 s8, 0x1100, 0
	v_med3_f32 v113, v163, -v255, v255
	v_med3_f32 v114, v167, -v255, v255
	v_cmp_eq_u32_e32 vcc, 0, v181
	v_add_u32_e32 v112, s8, v195
	v_cvt_scalef32_pk_fp8_f32 v118, v113, v114, s93
	s_and_b64 vcc, exec, vcc
	s_and_b32 s24, s58, 31
	ds_write_b16 v112, v115
	ds_write_b16 v112, v116 offset:68
	ds_write_b16 v112, v117 offset:136
	ds_write_b16 v112, v118 offset:204
	s_cbranch_vccnz .LBB4_809
	s_lshl_b32 s8, s24, 7
	s_lshl_b32 s9, s58, 6
	s_and_b32 s8, s8, 0xf00
	s_and_b32 s9, s9, 64
	s_or_b32 s20, s8, s9
	s_cbranch_execnz .LBB4_803

; DI void finishSM(f32x16& p0, f32x16& p1, float alpha, float& l_reg, bf16x8& pa0, bf16x8& pa1, bf16x8& pa2, bf16x8& pa3) {
; #pragma unroll
;     for (int r = 0; r < 16; ++r) p1[r] = __builtin_amdgcn_exp2f(p1[r]);
;     float ps = 0;
; #pragma unroll
;     for (int r = 0; r < 16; ++r) ps += p0[r];
; #pragma unroll
;     for (int r = 0; r < 16; ++r) ps += p1[r];
;     { auto rr = __builtin_amdgcn_permlane32_swap(__float_as_uint(ps), __float_as_uint(ps), false, false); ps = __uint_as_float(rr[0]) + __uint_as_float(rr[1]); }
;     l_reg = l_reg * alpha + ps;
;     ...
;     AT_PK4(p0, 0, pa0); AT_PK4(p0, 8, pa1); AT_PK4(p1, 0, pa2); AT_PK4(p1, 8, pa3);
;     ...
; }
; DI void qkt(f32x16& p0, f32x16& p1, const char* Ks, const bf16x8* qr, const f32x16& negm, int r32, int hi) {
; #pragma unroll
;     for (int d0 = 0; d0 < 4; ++d0) { const int cb = (d0 * 16 + hi * 8) * 2;
;         const bf16x8 b0 = *reinterpret_cast<const bf16x8*>(Ks + AT_KSWZ(r32, cb));
;         const bf16x8 b1 = *reinterpret_cast<const bf16x8*>(Ks + AT_KSWZ(32 + r32, cb));
;         p0 = __builtin_amdgcn_mfma_f32_32x32x16_bf16(b0, qr[d0], d0 == 0 ? negm : p0, 0, 0, 0);
;         p1 = __builtin_amdgcn_mfma_f32_32x32x16_bf16(b1, qr[d0], d0 == 0 ? negm : p1, 0, 0, 0); }
; }
.LBB4_849:
	s_lshl_b32 s26, s64, 13
	s_add_i32 s26, s26, 0
	v_add_u32_e32 v72, s26, v204
	v_add_u32_e32 v112, s26, v205
	v_add_u32_e32 v180, s26, v206
	s_waitcnt lgkmcnt(1)
	v_mfma_f32_32x32x16_bf16 v[128:143], v[64:67], v[156:159], v[80:95]
	ds_read_b128 v[64:67], v72 offset:49152
	ds_read_b128 v[72:75], v72 offset:53248
	ds_read_b128 v[76:79], v112 offset:49152
	ds_read_b128 v[220:223], v112 offset:53248
	s_add_u32 s66, s46, s28
	s_addc_u32 s67, s47, s29
	s_add_u32 s34, s66, 0x23808000
	s_addc_u32 s35, s67, 0
	s_add_u32 s76, s66, 0x2380a000
	s_add_u32 s74, s46, s24
	s_addc_u32 s75, s47, s25
	s_add_u32 s78, s74, 0x21804000
	s_addc_u32 s79, s75, 0
	s_lshl_b32 s92, s57, 14
	s_add_i32 s92, s92, s94
	s_mov_b32 m0, s92
	s_lshl_b32 s96, s57, 13
	global_load_lds_dwordx4 v249, s[34:35]
	s_addk_i32 s92, 0x400
	s_mov_b32 m0, s92
	s_add_i32 s96, s96, s95
	global_load_lds_dwordx4 v250, s[34:35]
	s_nop 0
	s_mov_b32 m0, s96
	s_nop 0
	global_load_lds_dwordx4 v251, s[78:79]
	v_exp_f32_e32 v182, v97
	v_exp_f32_e32 v213, v98
	v_exp_f32_e32 v214, v99
	v_exp_f32_e32 v219, v100
	v_exp_f32_e32 v228, v101
	s_waitcnt lgkmcnt(4)
	v_mfma_f32_32x32x16_bf16 v[112:127], v[68:71], v[156:159], v[80:95]
	ds_read_b128 v[68:71], v180 offset:49152
	ds_read_b128 v[224:227], v180 offset:53248
	v_exp_f32_e32 v180, v96
	v_cvt_pk_bf16_f32 v96, v216, v218
	v_cvt_pk_bf16_f32 v97, v179, v217
	v_cvt_pk_bf16_f32 v98, v177, v215
	v_cvt_pk_bf16_f32 v99, v176, v178
	s_waitcnt lgkmcnt(4)
	v_mfma_f32_32x32x16_bf16 v[112:127], v[72:75], v[152:155], v[112:127]
	v_add_f32_e32 v75, 0, v216
	v_add_f32_e32 v75, v218, v75
	v_add_f32_e32 v75, v217, v75
	v_add_f32_e32 v75, v215, v75
	v_add_f32_e32 v75, v176, v75
	v_mfma_f32_32x32x16_bf16 v[128:143], v[64:67], v[152:155], v[128:143]
	v_add_f32_e32 v75, v172, v75
	s_waitcnt lgkmcnt(3)
	v_mfma_f32_32x32x16_bf16 v[128:143], v[76:79], v[148:151], v[128:143]
	v_add_f32_e32 v75, v180, v75
	v_add_f32_e32 v75, v182, v75
	v_exp_f32_e32 v64, v102
	v_exp_f32_e32 v65, v103
	v_exp_f32_e32 v66, v104
	s_waitcnt lgkmcnt(2)
	v_mfma_f32_32x32x16_bf16 v[112:127], v[220:223], v[148:151], v[112:127]
	v_exp_f32_e32 v67, v105
	v_exp_f32_e32 v105, v106
	v_exp_f32_e32 v106, v107
	v_exp_f32_e32 v107, v108
	v_exp_f32_e32 v72, v109
	v_exp_f32_e32 v73, v110
	v_exp_f32_e32 v74, v111
	s_waitcnt lgkmcnt(1)
	v_mfma_f32_32x32x16_bf16 v[128:143], v[68:71], v[144:147], v[128:143]
	v_add_f32_e32 v68, v213, v75
	v_add_f32_e32 v68, v214, v68
	v_add_f32_e32 v68, v219, v68
	v_add_f32_e32 v68, v228, v68
	v_add_f32_e32 v68, v64, v68
	v_add_f32_e32 v68, v65, v68
	v_add_f32_e32 v68, v66, v68
	v_add_f32_e32 v68, v67, v68
	s_waitcnt lgkmcnt(0)
	v_mfma_f32_32x32x16_bf16 v[112:127], v[224:227], v[144:147], v[112:127]
	v_add_f32_e32 v68, v105, v68
	v_add_f32_e32 v68, v106, v68
	v_add_f32_e32 v68, v107, v68
	v_add_f32_e32 v68, v72, v68
	v_add_f32_e32 v68, v73, v68
	v_add_f32_e32 v211, v74, v68
	v_cvt_pk_bf16_f32 v100, v180, v182
	v_cvt_pk_bf16_f32 v101, v213, v214
	v_cvt_pk_bf16_f32 v102, v219, v228
	v_cvt_pk_bf16_f32 v103, v64, v65
	v_cvt_pk_bf16_f32 v104, v66, v67
	v_cvt_pk_bf16_f32 v105, v105, v106
	v_cvt_pk_bf16_f32 v106, v107, v72
	v_cvt_pk_bf16_f32 v107, v73, v74
	s_addc_u32 s77, s67, 0
	s_andn2_b64 vcc, exec, s[2:3]
	s_cbranch_vccnz .LBB4_851
	s_mov_b64 s[2:3], s[8:9]
	global_store_dwordx2 v188, v[184:185], s[2:3] nt

; #define AT_SBAR() __builtin_amdgcn_sched_barrier(0)
; template <int OFF> DI s16x4 tr_read(int vb) { s16x4 r; asm volatile("ds_read_b64_tr_b16 %0, %1 offset:%2" : "=&v"(r) : "v"(vb), "i"(OFF) : "memory"); return r; }
; template <int D0> DI void pv_one(f32x16& od, int vb, bf16x8 pa0, bf16x8 pa1, bf16x8 pa2, bf16x8 pa3) {
;     const s16x4 l0 = tr_read<v_rd_off(D0, 0, 0)>(vb), h0 = tr_read<v_rd_off(D0, 0, 1)>(vb), l1 = tr_read<v_rd_off(D0, 1, 0)>(vb), h1 = tr_read<v_rd_off(D0, 1, 1)>(vb);
;     const s16x4 l2 = tr_read<v_rd_off(D0, 2, 0)>(vb), h2 = tr_read<v_rd_off(D0, 2, 1)>(vb), l3 = tr_read<v_rd_off(D0, 3, 0)>(vb), h3 = tr_read<v_rd_off(D0, 3, 1)>(vb);
;     asm volatile("s_waitcnt lgkmcnt(0)" ::: "memory"); AT_SBAR();
;     ...
;     od = __builtin_amdgcn_mfma_f32_32x32x16_bf16(AT_PK(l0, h0), pa0, od, 0, 0, 0);
;     od = __builtin_amdgcn_mfma_f32_32x32x16_bf16(AT_PK(l1, h1), pa1, od, 0, 0, 0);
;     od = __builtin_amdgcn_mfma_f32_32x32x16_bf16(AT_PK(l2, h2), pa2, od, 0, 0, 0);
;     od = __builtin_amdgcn_mfma_f32_32x32x16_bf16(AT_PK(l3, h3), pa3, od, 0, 0, 0);
.LBB4_853:
	ds_read_b64_tr_b16 v[214:215], v182 offset:0x600
	ds_read_b64_tr_b16 v[216:217], v182 offset:0x700
	ds_read_b64_tr_b16 v[218:219], v182 offset:0x1600
	ds_read_b64_tr_b16 v[220:221], v182 offset:0x1700
	ds_read_b64_tr_b16 v[222:223], v182 offset:0x2600
	ds_read_b64_tr_b16 v[224:225], v182 offset:0x2700
	ds_read_b64_tr_b16 v[226:227], v182 offset:0x3600
	ds_read_b64_tr_b16 v[228:229], v182 offset:0x3700
	s_waitcnt lgkmcnt(0)
	v_mfma_f32_32x32x16_bf16 v[0:15], v[214:217], v[96:99], v[0:15]
	s_lshl_b32 s2, s57, 14
	s_lshl_b32 s3, s57, 13
	s_sub_i32 s76, s2, s3
	v_mfma_f32_32x32x16_bf16 v[0:15], v[218:221], v[108:111], v[0:15]
	s_andn2_b64 s[2:3], exec, s[30:31]
	s_andn2_b64 vcc, exec, s[30:31]
	v_mfma_f32_32x32x16_bf16 v[0:15], v[222:225], v[100:103], v[0:15]
	v_mfma_f32_32x32x16_bf16 v[0:15], v[226:229], v[104:107], v[0:15]
	v_add_f32_e32 v254, v170, v254
	v_add_f32_e32 v211, v254, v211
	s_cbranch_vccnz .LBB4_858
	s_waitcnt vmcnt(3)
	v_med3_f32 v97, v160, -v255, v255
	v_med3_f32 v98, v164, -v255, v255
	v_cvt_scalef32_pk_fp8_f32 v99, v97, v98, s93
	v_med3_f32 v97, v161, -v255, v255
	v_med3_f32 v98, v165, -v255, v255
	v_cvt_scalef32_pk_fp8_f32 v100, v97, v98, s93
	v_med3_f32 v97, v162, -v255, v255
	v_med3_f32 v98, v166, -v255, v255
	s_bitcmp1_b32 s58, 0
	v_cvt_scalef32_pk_fp8_f32 v101, v97, v98, s93
	s_cselect_b32 s8, 0x1100, 0
	v_med3_f32 v97, v163, -v255, v255
	v_med3_f32 v98, v167, -v255, v255
	v_cmp_eq_u32_e32 vcc, 0, v181
	v_add_u32_e32 v96, s8, v190
	v_cvt_scalef32_pk_fp8_f32 v102, v97, v98, s93
	s_and_b64 vcc, exec, vcc
	s_and_b32 s30, s58, 31
	ds_write_b16 v96, v99
	ds_write_b16 v96, v100 offset:68
	ds_write_b16 v96, v101 offset:136
	ds_write_b16 v96, v102 offset:204
	s_cbranch_vccnz .LBB4_882
	s_lshl_b32 s8, s30, 7
	s_lshl_b32 s9, s58, 6
	s_and_b32 s8, s8, 0xf00
	s_and_b32 s9, s9, 64
	s_or_b32 s26, s8, s9
	s_cbranch_execnz .LBB4_857

; DI void finishSM(f32x16& p0, f32x16& p1, float alpha, float& l_reg, bf16x8& pa0, bf16x8& pa1, bf16x8& pa2, bf16x8& pa3) {
; #pragma unroll
;     for (int r = 0; r < 16; ++r) p1[r] = __builtin_amdgcn_exp2f(p1[r]);
;     float ps = 0;
; #pragma unroll
;     for (int r = 0; r < 16; ++r) ps += p0[r];
; #pragma unroll
;     for (int r = 0; r < 16; ++r) ps += p1[r];
;     { auto rr = __builtin_amdgcn_permlane32_swap(__float_as_uint(ps), __float_as_uint(ps), false, false); ps = __uint_as_float(rr[0]) + __uint_as_float(rr[1]); }
;     l_reg = l_reg * alpha + ps;
;     ...
;     AT_PK4(p0, 0, pa0); AT_PK4(p0, 8, pa1); AT_PK4(p1, 0, pa2); AT_PK4(p1, 8, pa3);
;     ...
; }
; DI void qkt(f32x16& p0, f32x16& p1, const char* Ks, const bf16x8* qr, const f32x16& negm, int r32, int hi) {
; #pragma unroll
;     for (int d0 = 0; d0 < 4; ++d0) { const int cb = (d0 * 16 + hi * 8) * 2;
;         const bf16x8 b0 = *reinterpret_cast<const bf16x8*>(Ks + AT_KSWZ(r32, cb));
;         const bf16x8 b1 = *reinterpret_cast<const bf16x8*>(Ks + AT_KSWZ(32 + r32, cb));
;         p0 = __builtin_amdgcn_mfma_f32_32x32x16_bf16(b0, qr[d0], d0 == 0 ? negm : p0, 0, 0, 0);
;         p1 = __builtin_amdgcn_mfma_f32_32x32x16_bf16(b1, qr[d0], d0 == 0 ? negm : p1, 0, 0, 0); }
; }
.LBB4_870:
	v_exp_f32_e32 v182, v128
	v_exp_f32_e32 v230, v129
	v_exp_f32_e32 v231, v130
	v_exp_f32_e32 v232, v131
	v_exp_f32_e32 v233, v132
	v_exp_f32_e32 v234, v133
	v_exp_f32_e32 v235, v134
	v_exp_f32_e32 v236, v135
	v_exp_f32_e32 v237, v136
	v_exp_f32_e32 v238, v137
	v_exp_f32_e32 v239, v138
	v_exp_f32_e32 v240, v139
	v_exp_f32_e32 v241, v140
	v_exp_f32_e32 v242, v141
	v_exp_f32_e32 v243, v142
	v_exp_f32_e32 v244, v143
	v_add_u32_e32 v101, s76, v204
	v_add_u32_e32 v102, s76, v205
	v_add_u32_e32 v103, s76, v206
	ds_read_b128 v[172:175], v101 offset:49152
	ds_read_b128 v[176:179], v101 offset:53248
	ds_read_b128 v[214:217], v102 offset:49152
	ds_read_b128 v[218:221], v102 offset:53248
	ds_read_b128 v[222:225], v103 offset:49152
	ds_read_b128 v[226:229], v103 offset:53248
	v_exp_f32_e32 v112, v112
	v_exp_f32_e32 v113, v113
	v_exp_f32_e32 v114, v114
	s_waitcnt lgkmcnt(7)
	v_mfma_f32_32x32x16_bf16 v[128:143], v[96:99], v[156:159], v[80:95]
	s_add_u32 s34, s66, 0x2380c000
	s_addc_u32 s35, s67, 0
	s_add_u32 s66, s66, 0x2380e000
	s_addc_u32 s67, s67, 0
	s_add_u32 s74, s74, 0x21806000
	s_addc_u32 s75, s75, 0
	s_lshl_b32 s92, s63, 14
	s_add_i32 s92, s92, s94
	s_mov_b32 m0, s92
	s_lshl_b32 s96, s63, 13
	global_load_lds_dwordx4 v249, s[34:35]
	s_addk_i32 s92, 0x400
	s_mov_b32 m0, s92
	s_add_i32 s96, s96, s95
	global_load_lds_dwordx4 v250, s[34:35]
	s_nop 0
	s_mov_b32 m0, s96
	s_nop 0
	global_load_lds_dwordx4 v251, s[74:75]
	s_nop 0
	v_exp_f32_e32 v115, v115
	v_exp_f32_e32 v116, v116
	v_exp_f32_e32 v117, v117
	v_exp_f32_e32 v118, v118
	v_exp_f32_e32 v119, v119
	s_waitcnt lgkmcnt(6)
	v_mfma_f32_32x32x16_bf16 v[96:111], v[168:171], v[156:159], v[80:95]
	v_exp_f32_e32 v168, v120
	v_add_f32_e32 v120, 0, v182
	v_add_f32_e32 v120, v230, v120
	v_add_f32_e32 v120, v231, v120
	v_add_f32_e32 v120, v232, v120
	v_add_f32_e32 v120, v233, v120
	v_add_f32_e32 v120, v234, v120
	v_add_f32_e32 v120, v235, v120
	v_add_f32_e32 v120, v236, v120
	v_add_f32_e32 v120, v237, v120
	v_add_f32_e32 v120, v238, v120
	s_waitcnt lgkmcnt(5)
	v_mfma_f32_32x32x16_bf16 v[128:143], v[172:175], v[152:155], v[128:143]
	v_add_f32_e32 v120, v239, v120
	v_add_f32_e32 v120, v240, v120
	v_add_f32_e32 v120, v241, v120
	v_add_f32_e32 v120, v242, v120
	v_add_f32_e32 v120, v243, v120
	v_add_f32_e32 v120, v244, v120
	v_add_f32_e32 v120, v112, v120
	s_waitcnt lgkmcnt(4)
	v_mfma_f32_32x32x16_bf16 v[96:111], v[176:179], v[152:155], v[96:111]
	v_add_f32_e32 v120, v113, v120
	v_add_f32_e32 v120, v114, v120
	v_add_f32_e32 v120, v115, v120
	v_add_f32_e32 v120, v116, v120
	v_exp_f32_e32 v169, v121
	v_add_f32_e32 v120, v117, v120
	v_exp_f32_e32 v170, v122
	s_waitcnt lgkmcnt(3)
	v_mfma_f32_32x32x16_bf16 v[128:143], v[214:217], v[148:151], v[128:143]
	v_add_f32_e32 v120, v118, v120
	v_exp_f32_e32 v171, v123
	v_add_f32_e32 v120, v119, v120
	v_exp_f32_e32 v172, v124
	v_exp_f32_e32 v173, v125
	s_waitcnt lgkmcnt(2)
	v_mfma_f32_32x32x16_bf16 v[96:111], v[218:221], v[148:151], v[96:111]
	v_exp_f32_e32 v174, v126
	v_exp_f32_e32 v175, v127
	v_add_f32_e32 v120, v174, v120
	s_waitcnt lgkmcnt(1)
	v_mfma_f32_32x32x16_bf16 v[128:143], v[222:225], v[144:147], v[128:143]
	v_add_f32_e32 v213, v175, v120
	v_cvt_pk_bf16_f32 v120, v182, v230
	v_cvt_pk_bf16_f32 v121, v231, v232
	v_cvt_pk_bf16_f32 v122, v233, v234
	v_cvt_pk_bf16_f32 v123, v235, v236
	v_cvt_pk_bf16_f32 v124, v237, v238
	s_waitcnt lgkmcnt(0)
	v_mfma_f32_32x32x16_bf16 v[96:111], v[226:229], v[144:147], v[96:111]
	v_cvt_pk_bf16_f32 v125, v239, v240
	v_cvt_pk_bf16_f32 v126, v241, v242
	v_cvt_pk_bf16_f32 v127, v243, v244
	v_cvt_pk_bf16_f32 v112, v112, v113
	v_cvt_pk_bf16_f32 v113, v114, v115
	v_cvt_pk_bf16_f32 v114, v116, v117
	v_cvt_pk_bf16_f32 v115, v118, v119
	s_and_b64 vcc, exec, s[2:3]
	s_cbranch_vccnz .LBB4_872
	s_mov_b64 s[2:3], s[8:9]
	global_store_dwordx2 v188, v[184:185], s[2:3] nt

; #define AT_SBAR() __builtin_amdgcn_sched_barrier(0)
; template <int OFF> DI s16x4 tr_read(int vb) { s16x4 r; asm volatile("ds_read_b64_tr_b16 %0, %1 offset:%2" : "=&v"(r) : "v"(vb), "i"(OFF) : "memory"); return r; }
; template <int D0> DI void pv_one(f32x16& od, int vb, bf16x8 pa0, bf16x8 pa1, bf16x8 pa2, bf16x8 pa3) {
;     const s16x4 l0 = tr_read<v_rd_off(D0, 0, 0)>(vb), h0 = tr_read<v_rd_off(D0, 0, 1)>(vb), l1 = tr_read<v_rd_off(D0, 1, 0)>(vb), h1 = tr_read<v_rd_off(D0, 1, 1)>(vb);
;     const s16x4 l2 = tr_read<v_rd_off(D0, 2, 0)>(vb), h2 = tr_read<v_rd_off(D0, 2, 1)>(vb), l3 = tr_read<v_rd_off(D0, 3, 0)>(vb), h3 = tr_read<v_rd_off(D0, 3, 1)>(vb);
;     asm volatile("s_waitcnt lgkmcnt(0)" ::: "memory"); AT_SBAR();
;     ...
;     od = __builtin_amdgcn_mfma_f32_32x32x16_bf16(AT_PK(l0, h0), pa0, od, 0, 0, 0);
;     od = __builtin_amdgcn_mfma_f32_32x32x16_bf16(AT_PK(l1, h1), pa1, od, 0, 0, 0);
;     od = __builtin_amdgcn_mfma_f32_32x32x16_bf16(AT_PK(l2, h2), pa2, od, 0, 0, 0);
;     od = __builtin_amdgcn_mfma_f32_32x32x16_bf16(AT_PK(l3, h3), pa3, od, 0, 0, 0);
.LBB4_873:
	ds_read_b64_tr_b16 v[216:217], v215 offset:0x600
	ds_read_b64_tr_b16 v[218:219], v215 offset:0x700
	ds_read_b64_tr_b16 v[220:221], v215 offset:0x1600
	ds_read_b64_tr_b16 v[222:223], v215 offset:0x1700
	ds_read_b64_tr_b16 v[224:225], v215 offset:0x2600
	ds_read_b64_tr_b16 v[226:227], v215 offset:0x2700
	ds_read_b64_tr_b16 v[228:229], v215 offset:0x3600
	ds_read_b64_tr_b16 v[230:231], v215 offset:0x3700
	s_waitcnt lgkmcnt(0)
	v_mfma_f32_32x32x16_bf16 v[0:15], v[216:219], v[120:123], v[0:15]
	s_add_i32 s2, s65, 0
	s_mov_b32 s26, 0
	s_andn2_b64 vcc, exec, s[30:31]
	v_mfma_f32_32x32x16_bf16 v[0:15], v[220:223], v[124:127], v[0:15]
	v_mfma_f32_32x32x16_bf16 v[0:15], v[224:227], v[112:115], v[0:15]
	s_andn2_b64 s[2:3], exec, s[30:31]
	v_mfma_f32_32x32x16_bf16 v[0:15], v[228:231], v[116:119], v[0:15]
	v_add_f32_e32 v254, v173, v254
	v_add_f32_e32 v213, v254, v213
	s_cbranch_vccnz .LBB4_878
	s_waitcnt vmcnt(3)
	v_med3_f32 v113, v160, -v255, v255
	v_med3_f32 v114, v164, -v255, v255
	v_cvt_scalef32_pk_fp8_f32 v115, v113, v114, s93
	v_med3_f32 v113, v161, -v255, v255
	v_med3_f32 v114, v165, -v255, v255
	v_cvt_scalef32_pk_fp8_f32 v116, v113, v114, s93
	v_med3_f32 v113, v162, -v255, v255
	v_med3_f32 v114, v166, -v255, v255
	s_bitcmp1_b32 s58, 0
	v_cvt_scalef32_pk_fp8_f32 v117, v113, v114, s93
	s_cselect_b32 s8, 0x1100, 0
	v_med3_f32 v113, v163, -v255, v255
	v_med3_f32 v114, v167, -v255, v255
	v_cmp_eq_u32_e32 vcc, 0, v181
	v_add_u32_e32 v112, s8, v190
	v_cvt_scalef32_pk_fp8_f32 v118, v113, v114, s93
	s_and_b64 vcc, exec, vcc
	s_and_b32 s34, s58, 31
	ds_write_b16 v112, v115
	ds_write_b16 v112, v116 offset:68
	ds_write_b16 v112, v117 offset:136
	ds_write_b16 v112, v118 offset:204
	s_cbranch_vccnz .LBB4_883
	s_lshl_b32 s8, s34, 7
	s_lshl_b32 s9, s58, 6
	s_and_b32 s8, s8, 0xf00
	s_and_b32 s9, s9, 64
	s_or_b32 s26, s8, s9
	s_cbranch_execnz .LBB4_877

; DI void finishSM(f32x16& p0, f32x16& p1, float alpha, float& l_reg, bf16x8& pa0, bf16x8& pa1, bf16x8& pa2, bf16x8& pa3) {
; #pragma unroll
;     for (int r = 0; r < 16; ++r) p1[r] = __builtin_amdgcn_exp2f(p1[r]);
;     float ps = 0;
; #pragma unroll
;     for (int r = 0; r < 16; ++r) ps += p0[r];
; #pragma unroll
;     for (int r = 0; r < 16; ++r) ps += p1[r];
;     { auto rr = __builtin_amdgcn_permlane32_swap(__float_as_uint(ps), __float_as_uint(ps), false, false); ps = __uint_as_float(rr[0]) + __uint_as_float(rr[1]); }
;     l_reg = l_reg * alpha + ps;
;     ...
;     AT_PK4(p0, 0, pa0); AT_PK4(p0, 8, pa1); AT_PK4(p1, 0, pa2); AT_PK4(p1, 8, pa3);
;     ...
; }
; DI void qkt(f32x16& p0, f32x16& p1, const char* Ks, const bf16x8* qr, const f32x16& negm, int r32, int hi) {
; #pragma unroll
;     for (int d0 = 0; d0 < 4; ++d0) { const int cb = (d0 * 16 + hi * 8) * 2;
;         const bf16x8 b0 = *reinterpret_cast<const bf16x8*>(Ks + AT_KSWZ(r32, cb));
;         const bf16x8 b1 = *reinterpret_cast<const bf16x8*>(Ks + AT_KSWZ(32 + r32, cb));
;         p0 = __builtin_amdgcn_mfma_f32_32x32x16_bf16(b0, qr[d0], d0 == 0 ? negm : p0, 0, 0, 0);
;         p1 = __builtin_amdgcn_mfma_f32_32x32x16_bf16(b1, qr[d0], d0 == 0 ? negm : p1, 0, 0, 0); }
; }
.LBB4_923:
	s_lshl_b32 s18, s30, 13
	s_add_i32 s18, s18, 0
	v_add_u32_e32 v72, s18, v208
	v_add_u32_e32 v112, s18, v209
	v_add_u32_e32 v180, s18, v210
	s_waitcnt lgkmcnt(1)
	v_mfma_f32_32x32x16_bf16 v[128:143], v[64:67], v[156:159], v[80:95]
	ds_read_b128 v[64:67], v72 offset:49152
	ds_read_b128 v[72:75], v72 offset:53248
	ds_read_b128 v[76:79], v112 offset:49152
	ds_read_b128 v[224:227], v112 offset:53248
	s_add_u32 s34, s46, s16
	s_addc_u32 s35, s47, s17
	s_add_u32 s24, s34, 0x23808000
	s_addc_u32 s25, s35, 0
	s_add_u32 s54, s34, 0x2380a000
	s_add_u32 s42, s46, s20
	s_addc_u32 s43, s47, s21
	s_add_u32 s56, s42, 0x21884000
	s_addc_u32 s57, s43, 0
	s_lshl_b32 s92, s15, 14
	s_add_i32 s92, s92, s94
	s_mov_b32 m0, s92
	s_lshl_b32 s96, s15, 13
	global_load_lds_dwordx4 v249, s[24:25]
	s_addk_i32 s92, 0x400
	s_mov_b32 m0, s92
	s_add_i32 s96, s96, s95
	global_load_lds_dwordx4 v250, s[24:25]
	s_nop 0
	s_mov_b32 m0, s96
	s_nop 0
	global_load_lds_dwordx4 v251, s[56:57]
	v_exp_f32_e32 v182, v97
	v_exp_f32_e32 v217, v98
	v_exp_f32_e32 v218, v99
	v_exp_f32_e32 v223, v100
	v_exp_f32_e32 v232, v101
	s_waitcnt lgkmcnt(4)
	v_mfma_f32_32x32x16_bf16 v[112:127], v[68:71], v[156:159], v[80:95]
	ds_read_b128 v[68:71], v180 offset:49152
	ds_read_b128 v[228:231], v180 offset:53248
	v_exp_f32_e32 v180, v96
	v_cvt_pk_bf16_f32 v96, v220, v222
	v_cvt_pk_bf16_f32 v97, v179, v221
	v_cvt_pk_bf16_f32 v98, v177, v219
	v_cvt_pk_bf16_f32 v99, v176, v178
	s_waitcnt lgkmcnt(4)
	v_mfma_f32_32x32x16_bf16 v[112:127], v[72:75], v[152:155], v[112:127]
	v_add_f32_e32 v75, 0, v220
	v_add_f32_e32 v75, v222, v75
	v_add_f32_e32 v75, v221, v75
	v_add_f32_e32 v75, v219, v75
	v_add_f32_e32 v75, v176, v75
	v_mfma_f32_32x32x16_bf16 v[128:143], v[64:67], v[152:155], v[128:143]
	v_add_f32_e32 v75, v172, v75
	s_waitcnt lgkmcnt(3)
	v_mfma_f32_32x32x16_bf16 v[128:143], v[76:79], v[148:151], v[128:143]
	v_add_f32_e32 v75, v180, v75
	v_add_f32_e32 v75, v182, v75
	v_exp_f32_e32 v64, v102
	v_exp_f32_e32 v65, v103
	v_exp_f32_e32 v66, v104
	s_waitcnt lgkmcnt(2)
	v_mfma_f32_32x32x16_bf16 v[112:127], v[224:227], v[148:151], v[112:127]
	v_exp_f32_e32 v67, v105
	v_exp_f32_e32 v105, v106
	v_exp_f32_e32 v106, v107
	v_exp_f32_e32 v107, v108
	v_exp_f32_e32 v72, v109
	v_exp_f32_e32 v73, v110
	v_exp_f32_e32 v74, v111
	s_waitcnt lgkmcnt(1)
	v_mfma_f32_32x32x16_bf16 v[128:143], v[68:71], v[144:147], v[128:143]
	v_add_f32_e32 v68, v217, v75
	v_add_f32_e32 v68, v218, v68
	v_add_f32_e32 v68, v223, v68
	v_add_f32_e32 v68, v232, v68
	v_add_f32_e32 v68, v64, v68
	v_add_f32_e32 v68, v65, v68
	v_add_f32_e32 v68, v66, v68
	v_add_f32_e32 v68, v67, v68
	s_waitcnt lgkmcnt(0)
	v_mfma_f32_32x32x16_bf16 v[112:127], v[228:231], v[144:147], v[112:127]
	v_add_f32_e32 v68, v105, v68
	v_add_f32_e32 v68, v106, v68
	v_add_f32_e32 v68, v107, v68
	v_add_f32_e32 v68, v72, v68
	v_add_f32_e32 v68, v73, v68
	v_add_f32_e32 v215, v74, v68
	v_cvt_pk_bf16_f32 v100, v180, v182
	v_cvt_pk_bf16_f32 v101, v217, v218
	v_cvt_pk_bf16_f32 v102, v223, v232
	v_cvt_pk_bf16_f32 v103, v64, v65
	v_cvt_pk_bf16_f32 v104, v66, v67
	v_cvt_pk_bf16_f32 v105, v105, v106
	v_cvt_pk_bf16_f32 v106, v107, v72
	v_cvt_pk_bf16_f32 v107, v73, v74
	s_addc_u32 s55, s35, 0
	s_andn2_b64 vcc, exec, s[2:3]
	s_cbranch_vccnz .LBB4_925
	s_mov_b64 s[2:3], s[8:9]
	global_store_dwordx2 v193, v[184:185], s[2:3] nt

; #define AT_SBAR() __builtin_amdgcn_sched_barrier(0)
; template <int OFF> DI s16x4 tr_read(int vb) { s16x4 r; asm volatile("ds_read_b64_tr_b16 %0, %1 offset:%2" : "=&v"(r) : "v"(vb), "i"(OFF) : "memory"); return r; }
; template <int D0> DI void pv_one(f32x16& od, int vb, bf16x8 pa0, bf16x8 pa1, bf16x8 pa2, bf16x8 pa3) {
;     const s16x4 l0 = tr_read<v_rd_off(D0, 0, 0)>(vb), h0 = tr_read<v_rd_off(D0, 0, 1)>(vb), l1 = tr_read<v_rd_off(D0, 1, 0)>(vb), h1 = tr_read<v_rd_off(D0, 1, 1)>(vb);
;     const s16x4 l2 = tr_read<v_rd_off(D0, 2, 0)>(vb), h2 = tr_read<v_rd_off(D0, 2, 1)>(vb), l3 = tr_read<v_rd_off(D0, 3, 0)>(vb), h3 = tr_read<v_rd_off(D0, 3, 1)>(vb);
;     asm volatile("s_waitcnt lgkmcnt(0)" ::: "memory"); AT_SBAR();
;     ...
;     od = __builtin_amdgcn_mfma_f32_32x32x16_bf16(AT_PK(l0, h0), pa0, od, 0, 0, 0);
;     od = __builtin_amdgcn_mfma_f32_32x32x16_bf16(AT_PK(l1, h1), pa1, od, 0, 0, 0);
;     od = __builtin_amdgcn_mfma_f32_32x32x16_bf16(AT_PK(l2, h2), pa2, od, 0, 0, 0);
;     od = __builtin_amdgcn_mfma_f32_32x32x16_bf16(AT_PK(l3, h3), pa3, od, 0, 0, 0);
.LBB4_927:
	ds_read_b64_tr_b16 v[218:219], v182 offset:0x600
	ds_read_b64_tr_b16 v[220:221], v182 offset:0x700
	ds_read_b64_tr_b16 v[222:223], v182 offset:0x1600
	ds_read_b64_tr_b16 v[224:225], v182 offset:0x1700
	ds_read_b64_tr_b16 v[226:227], v182 offset:0x2600
	ds_read_b64_tr_b16 v[228:229], v182 offset:0x2700
	ds_read_b64_tr_b16 v[230:231], v182 offset:0x3600
	ds_read_b64_tr_b16 v[232:233], v182 offset:0x3700
	s_waitcnt lgkmcnt(0)
	v_mfma_f32_32x32x16_bf16 v[0:15], v[218:221], v[96:99], v[0:15]
	s_lshl_b32 s2, s15, 14
	s_lshl_b32 s3, s15, 13
	s_sub_i32 s54, s2, s3
	v_mfma_f32_32x32x16_bf16 v[0:15], v[222:225], v[108:111], v[0:15]
	s_andn2_b64 s[2:3], exec, s[22:23]
	s_andn2_b64 vcc, exec, s[22:23]
	v_mfma_f32_32x32x16_bf16 v[0:15], v[226:229], v[100:103], v[0:15]
	v_mfma_f32_32x32x16_bf16 v[0:15], v[230:233], v[104:107], v[0:15]
	v_add_f32_e32 v254, v170, v254
	v_add_f32_e32 v215, v254, v215
	s_cbranch_vccnz .LBB4_932
	s_waitcnt vmcnt(3)
	v_med3_f32 v97, v160, -v255, v255
	v_med3_f32 v98, v164, -v255, v255
	v_cvt_scalef32_pk_fp8_f32 v99, v97, v98, s93
	v_med3_f32 v97, v161, -v255, v255
	v_med3_f32 v98, v165, -v255, v255
	v_cvt_scalef32_pk_fp8_f32 v100, v97, v98, s93
	v_med3_f32 v97, v162, -v255, v255
	v_med3_f32 v98, v166, -v255, v255
	s_bitcmp1_b32 s58, 0
	v_cvt_scalef32_pk_fp8_f32 v101, v97, v98, s93
	s_cselect_b32 s8, 0x1100, 0
	v_med3_f32 v97, v163, -v255, v255
	v_med3_f32 v98, v167, -v255, v255
	v_cmp_eq_u32_e32 vcc, 0, v181
	v_add_u32_e32 v96, s8, v195
	v_cvt_scalef32_pk_fp8_f32 v102, v97, v98, s93
	s_and_b64 vcc, exec, vcc
	s_and_b32 s22, s58, 31
	ds_write_b16 v96, v99
	ds_write_b16 v96, v100 offset:68
	ds_write_b16 v96, v101 offset:136
	ds_write_b16 v96, v102 offset:204
	s_cbranch_vccnz .LBB4_956
	s_lshl_b32 s8, s22, 7
	s_lshl_b32 s9, s58, 6
	s_and_b32 s8, s8, 0xf00
	s_and_b32 s9, s9, 64
	s_or_b32 s18, s8, s9
	s_cbranch_execnz .LBB4_931

; DI void finishSM(f32x16& p0, f32x16& p1, float alpha, float& l_reg, bf16x8& pa0, bf16x8& pa1, bf16x8& pa2, bf16x8& pa3) {
; #pragma unroll
;     for (int r = 0; r < 16; ++r) p1[r] = __builtin_amdgcn_exp2f(p1[r]);
;     float ps = 0;
; #pragma unroll
;     for (int r = 0; r < 16; ++r) ps += p0[r];
; #pragma unroll
;     for (int r = 0; r < 16; ++r) ps += p1[r];
;     { auto rr = __builtin_amdgcn_permlane32_swap(__float_as_uint(ps), __float_as_uint(ps), false, false); ps = __uint_as_float(rr[0]) + __uint_as_float(rr[1]); }
;     l_reg = l_reg * alpha + ps;
;     ...
;     AT_PK4(p0, 0, pa0); AT_PK4(p0, 8, pa1); AT_PK4(p1, 0, pa2); AT_PK4(p1, 8, pa3);
;     ...
; }
; DI void qkt(f32x16& p0, f32x16& p1, const char* Ks, const bf16x8* qr, const f32x16& negm, int r32, int hi) {
; #pragma unroll
;     for (int d0 = 0; d0 < 4; ++d0) { const int cb = (d0 * 16 + hi * 8) * 2;
;         const bf16x8 b0 = *reinterpret_cast<const bf16x8*>(Ks + AT_KSWZ(r32, cb));
;         const bf16x8 b1 = *reinterpret_cast<const bf16x8*>(Ks + AT_KSWZ(32 + r32, cb));
;         p0 = __builtin_amdgcn_mfma_f32_32x32x16_bf16(b0, qr[d0], d0 == 0 ? negm : p0, 0, 0, 0);
;         p1 = __builtin_amdgcn_mfma_f32_32x32x16_bf16(b1, qr[d0], d0 == 0 ? negm : p1, 0, 0, 0); }
; }
.LBB4_944:
	v_exp_f32_e32 v182, v128
	v_exp_f32_e32 v234, v129
	v_exp_f32_e32 v235, v130
	v_exp_f32_e32 v236, v131
	v_exp_f32_e32 v237, v132
	v_exp_f32_e32 v238, v133
	v_exp_f32_e32 v239, v134
	v_exp_f32_e32 v240, v135
	v_exp_f32_e32 v241, v136
	v_exp_f32_e32 v242, v137
	v_exp_f32_e32 v243, v138
	v_exp_f32_e32 v244, v139
	v_exp_f32_e32 v245, v140
	v_exp_f32_e32 v246, v141
	v_exp_f32_e32 v247, v142
	v_exp_f32_e32 v248, v143
	v_add_u32_e32 v101, s54, v208
	v_add_u32_e32 v102, s54, v209
	v_add_u32_e32 v103, s54, v210
	ds_read_b128 v[172:175], v101 offset:49152
	ds_read_b128 v[176:179], v101 offset:53248
	ds_read_b128 v[218:221], v102 offset:49152
	ds_read_b128 v[222:225], v102 offset:53248
	ds_read_b128 v[226:229], v103 offset:49152
	ds_read_b128 v[230:233], v103 offset:53248
	v_exp_f32_e32 v112, v112
	v_exp_f32_e32 v113, v113
	v_exp_f32_e32 v114, v114
	s_waitcnt lgkmcnt(7)
	v_mfma_f32_32x32x16_bf16 v[128:143], v[96:99], v[156:159], v[80:95]
	s_add_u32 s24, s34, 0x2380c000
	s_addc_u32 s25, s35, 0
	s_add_u32 s34, s34, 0x2380e000
	s_addc_u32 s35, s35, 0
	s_add_u32 s42, s42, 0x21886000
	s_addc_u32 s43, s43, 0
	s_lshl_b32 s92, s29, 14
	s_add_i32 s92, s92, s94
	s_mov_b32 m0, s92
	s_lshl_b32 s96, s29, 13
	global_load_lds_dwordx4 v249, s[24:25]
	s_addk_i32 s92, 0x400
	s_mov_b32 m0, s92
	s_add_i32 s96, s96, s95
	global_load_lds_dwordx4 v250, s[24:25]
	s_nop 0
	s_mov_b32 m0, s96
	s_nop 0
	global_load_lds_dwordx4 v251, s[42:43]
	s_nop 0
	v_exp_f32_e32 v115, v115
	v_exp_f32_e32 v116, v116
	v_exp_f32_e32 v117, v117
	v_exp_f32_e32 v118, v118
	v_exp_f32_e32 v119, v119
	s_waitcnt lgkmcnt(6)
	v_mfma_f32_32x32x16_bf16 v[96:111], v[168:171], v[156:159], v[80:95]
	v_exp_f32_e32 v168, v120
	v_add_f32_e32 v120, 0, v182
	v_add_f32_e32 v120, v234, v120
	v_add_f32_e32 v120, v235, v120
	v_add_f32_e32 v120, v236, v120
	v_add_f32_e32 v120, v237, v120
	v_add_f32_e32 v120, v238, v120
	v_add_f32_e32 v120, v239, v120
	v_add_f32_e32 v120, v240, v120
	v_add_f32_e32 v120, v241, v120
	v_add_f32_e32 v120, v242, v120
	s_waitcnt lgkmcnt(5)
	v_mfma_f32_32x32x16_bf16 v[128:143], v[172:175], v[152:155], v[128:143]
	v_add_f32_e32 v120, v243, v120
	v_add_f32_e32 v120, v244, v120
	v_add_f32_e32 v120, v245, v120
	v_add_f32_e32 v120, v246, v120
	v_add_f32_e32 v120, v247, v120
	v_add_f32_e32 v120, v248, v120
	v_add_f32_e32 v120, v112, v120
	s_waitcnt lgkmcnt(4)
	v_mfma_f32_32x32x16_bf16 v[96:111], v[176:179], v[152:155], v[96:111]
	v_add_f32_e32 v120, v113, v120
	v_add_f32_e32 v120, v114, v120
	v_add_f32_e32 v120, v115, v120
	v_add_f32_e32 v120, v116, v120
	v_exp_f32_e32 v169, v121
	v_add_f32_e32 v120, v117, v120
	v_exp_f32_e32 v170, v122
	s_waitcnt lgkmcnt(3)
	v_mfma_f32_32x32x16_bf16 v[128:143], v[218:221], v[148:151], v[128:143]
	v_add_f32_e32 v120, v118, v120
	v_exp_f32_e32 v171, v123
	v_add_f32_e32 v120, v119, v120
	v_exp_f32_e32 v172, v124
	v_exp_f32_e32 v173, v125
	s_waitcnt lgkmcnt(2)
	v_mfma_f32_32x32x16_bf16 v[96:111], v[222:225], v[148:151], v[96:111]
	v_exp_f32_e32 v174, v126
	v_exp_f32_e32 v175, v127
	v_add_f32_e32 v120, v174, v120
	s_waitcnt lgkmcnt(1)
	v_mfma_f32_32x32x16_bf16 v[128:143], v[226:229], v[144:147], v[128:143]
	v_add_f32_e32 v217, v175, v120
	v_cvt_pk_bf16_f32 v120, v182, v234
	v_cvt_pk_bf16_f32 v121, v235, v236
	v_cvt_pk_bf16_f32 v122, v237, v238
	v_cvt_pk_bf16_f32 v123, v239, v240
	v_cvt_pk_bf16_f32 v124, v241, v242
	s_waitcnt lgkmcnt(0)
	v_mfma_f32_32x32x16_bf16 v[96:111], v[230:233], v[144:147], v[96:111]
	v_cvt_pk_bf16_f32 v125, v243, v244
	v_cvt_pk_bf16_f32 v126, v245, v246
	v_cvt_pk_bf16_f32 v127, v247, v248
	v_cvt_pk_bf16_f32 v112, v112, v113
	v_cvt_pk_bf16_f32 v113, v114, v115
	v_cvt_pk_bf16_f32 v114, v116, v117
	v_cvt_pk_bf16_f32 v115, v118, v119
	s_and_b64 vcc, exec, s[2:3]
	s_cbranch_vccnz .LBB4_946
	s_mov_b64 s[2:3], s[8:9]
	global_store_dwordx2 v193, v[184:185], s[2:3] nt

; #define AT_SBAR() __builtin_amdgcn_sched_barrier(0)
; template <int OFF> DI s16x4 tr_read(int vb) { s16x4 r; asm volatile("ds_read_b64_tr_b16 %0, %1 offset:%2" : "=&v"(r) : "v"(vb), "i"(OFF) : "memory"); return r; }
; template <int D0> DI void pv_one(f32x16& od, int vb, bf16x8 pa0, bf16x8 pa1, bf16x8 pa2, bf16x8 pa3) {
;     const s16x4 l0 = tr_read<v_rd_off(D0, 0, 0)>(vb), h0 = tr_read<v_rd_off(D0, 0, 1)>(vb), l1 = tr_read<v_rd_off(D0, 1, 0)>(vb), h1 = tr_read<v_rd_off(D0, 1, 1)>(vb);
;     const s16x4 l2 = tr_read<v_rd_off(D0, 2, 0)>(vb), h2 = tr_read<v_rd_off(D0, 2, 1)>(vb), l3 = tr_read<v_rd_off(D0, 3, 0)>(vb), h3 = tr_read<v_rd_off(D0, 3, 1)>(vb);
;     asm volatile("s_waitcnt lgkmcnt(0)" ::: "memory"); AT_SBAR();
;     ...
;     od = __builtin_amdgcn_mfma_f32_32x32x16_bf16(AT_PK(l0, h0), pa0, od, 0, 0, 0);
;     od = __builtin_amdgcn_mfma_f32_32x32x16_bf16(AT_PK(l1, h1), pa1, od, 0, 0, 0);
;     od = __builtin_amdgcn_mfma_f32_32x32x16_bf16(AT_PK(l2, h2), pa2, od, 0, 0, 0);
;     od = __builtin_amdgcn_mfma_f32_32x32x16_bf16(AT_PK(l3, h3), pa3, od, 0, 0, 0);
.LBB4_947:
	ds_read_b64_tr_b16 v[220:221], v219 offset:0x600
	ds_read_b64_tr_b16 v[222:223], v219 offset:0x700
	ds_read_b64_tr_b16 v[224:225], v219 offset:0x1600
	ds_read_b64_tr_b16 v[226:227], v219 offset:0x1700
	ds_read_b64_tr_b16 v[228:229], v219 offset:0x2600
	ds_read_b64_tr_b16 v[230:231], v219 offset:0x2700
	ds_read_b64_tr_b16 v[232:233], v219 offset:0x3600
	ds_read_b64_tr_b16 v[234:235], v219 offset:0x3700
	s_waitcnt lgkmcnt(0)
	v_mfma_f32_32x32x16_bf16 v[0:15], v[220:223], v[120:123], v[0:15]
	s_add_i32 s2, s31, 0
	s_mov_b32 s18, 0
	s_andn2_b64 vcc, exec, s[22:23]
	v_mfma_f32_32x32x16_bf16 v[0:15], v[224:227], v[124:127], v[0:15]
	v_mfma_f32_32x32x16_bf16 v[0:15], v[228:231], v[112:115], v[0:15]
	s_andn2_b64 s[2:3], exec, s[22:23]
	v_mfma_f32_32x32x16_bf16 v[0:15], v[232:235], v[116:119], v[0:15]
	v_add_f32_e32 v254, v173, v254
	v_add_f32_e32 v217, v254, v217
	s_cbranch_vccnz .LBB4_952
	s_waitcnt vmcnt(3)
	v_med3_f32 v113, v160, -v255, v255
	v_med3_f32 v114, v164, -v255, v255
	v_cvt_scalef32_pk_fp8_f32 v115, v113, v114, s93
	v_med3_f32 v113, v161, -v255, v255
	v_med3_f32 v114, v165, -v255, v255
	v_cvt_scalef32_pk_fp8_f32 v116, v113, v114, s93
	v_med3_f32 v113, v162, -v255, v255
	v_med3_f32 v114, v166, -v255, v255
	s_bitcmp1_b32 s58, 0
	v_cvt_scalef32_pk_fp8_f32 v117, v113, v114, s93
	s_cselect_b32 s8, 0x1100, 0
	v_med3_f32 v113, v163, -v255, v255
	v_med3_f32 v114, v167, -v255, v255
	v_cmp_eq_u32_e32 vcc, 0, v181
	v_add_u32_e32 v112, s8, v195
	v_cvt_scalef32_pk_fp8_f32 v118, v113, v114, s93
	s_and_b64 vcc, exec, vcc
	s_and_b32 s24, s58, 31
	ds_write_b16 v112, v115
	ds_write_b16 v112, v116 offset:68
	ds_write_b16 v112, v117 offset:136
	ds_write_b16 v112, v118 offset:204
	s_cbranch_vccnz .LBB4_957
	s_lshl_b32 s8, s24, 7
	s_lshl_b32 s9, s58, 6
	s_and_b32 s8, s8, 0xf00
	s_and_b32 s9, s9, 64
	s_or_b32 s18, s8, s9
	s_cbranch_execnz .LBB4_951
